# top-k sampled bracket with a 9-bit (one octave) prefix
# speedup vs baseline: 1.0058x; 1.0027x over previous
.Ltk0_a32:
	s_or_b32 s6, s4, s5
	v_cmp_le_u32_e64 s[8:9], s6, v179
	v_cmp_le_u32_e64 s[12:13], s6, v187
	v_cmp_le_u32_e64 s[16:17], s6, v192
	v_cndmask_b32_e64 v8, 0, 1, s[8:9]
	v_cmp_le_u32_e64 s[8:9], s6, v196
	v_addc_co_u32_e64 v8, s[20:21], 0, v8, s[12:13]
	v_cmp_le_u32_e64 s[12:13], s6, v207
	v_addc_co_u32_e64 v8, s[20:21], 0, v8, s[16:17]
	v_cmp_le_u32_e64 s[16:17], s6, v211
	v_addc_co_u32_e64 v8, s[20:21], 0, v8, s[8:9]
	v_cmp_le_u32_e64 s[8:9], s6, v215
	v_addc_co_u32_e64 v8, s[20:21], 0, v8, s[12:13]
	v_cmp_le_u32_e64 s[12:13], s6, v220
	v_addc_co_u32_e64 v8, s[20:21], 0, v8, s[16:17]
	v_addc_co_u32_e64 v8, s[20:21], 0, v8, s[8:9]
	v_addc_co_u32_e64 v8, s[20:21], 0, v8, s[12:13]
	v_and_b32_e32 v9, 8, v8
	v_cmp_ne_u32_e64 s[18:19], 0, v9
	v_and_b32_e32 v9, 4, v8
	v_cmp_ne_u32_e64 s[16:17], 0, v9
	v_and_b32_e32 v9, 2, v8
	v_cmp_ne_u32_e64 s[12:13], 0, v9
	v_and_b32_e32 v9, 1, v8
	v_cmp_ne_u32_e64 s[8:9], 0, v9
	s_bcnt1_i32_b64 s7, s[18:19]
	s_bcnt1_i32_b64 s3, s[16:17]
	s_lshl1_add_u32 s7, s7, s3
	s_bcnt1_i32_b64 s3, s[12:13]
	s_lshl1_add_u32 s7, s7, s3
	s_bcnt1_i32_b64 s3, s[8:9]
	s_lshl1_add_u32 s7, s7, s3
	s_cmp_lt_u32 s7, s11
	s_cselect_b32 s4, s4, s6
	s_lshr_b32 s5, s5, 1
	s_cmp_lg_u32 s5, 0x400000
	s_cbranch_scc1 .Ltk0_a32
	s_mov_b32 s10, s4
	s_add_u32 s6, s4, 0x800000
	s_cbranch_scc1 .Ltk0_f32
	s_mov_b32 s5, 0

.Ltk0_c32:
	s_cmpk_lt_u32 s7, 0x100
	s_cbranch_scc1 .Ltk0_f32
	s_mov_b32 s4, s10
	s_cmpk_eq_u32 s7, 0x100
	s_cbranch_scc1 .Ltk0_x32
	s_mov_b32 s5, 0x400000
	s_branch .Ltk0_l32

.Ltk0_a28:
	s_or_b32 s6, s4, s5
	v_cmp_le_u32_e64 s[8:9], s6, v179
	v_cmp_le_u32_e64 s[12:13], s6, v187
	v_cmp_le_u32_e64 s[16:17], s6, v192
	v_cndmask_b32_e64 v8, 0, 1, s[8:9]
	v_cmp_le_u32_e64 s[8:9], s6, v196
	v_addc_co_u32_e64 v8, s[20:21], 0, v8, s[12:13]
	v_cmp_le_u32_e64 s[12:13], s6, v207
	v_addc_co_u32_e64 v8, s[20:21], 0, v8, s[16:17]
	v_cmp_le_u32_e64 s[16:17], s6, v211
	v_addc_co_u32_e64 v8, s[20:21], 0, v8, s[8:9]
	v_cmp_le_u32_e64 s[8:9], s6, v215
	v_addc_co_u32_e64 v8, s[20:21], 0, v8, s[12:13]
	v_addc_co_u32_e64 v8, s[20:21], 0, v8, s[16:17]
	v_addc_co_u32_e64 v8, s[20:21], 0, v8, s[8:9]
	v_and_b32_e32 v9, 4, v8
	v_cmp_ne_u32_e64 s[16:17], 0, v9
	v_and_b32_e32 v9, 2, v8
	v_cmp_ne_u32_e64 s[12:13], 0, v9
	v_and_b32_e32 v9, 1, v8
	v_cmp_ne_u32_e64 s[8:9], 0, v9
	s_bcnt1_i32_b64 s7, s[16:17]
	s_bcnt1_i32_b64 s3, s[12:13]
	s_lshl1_add_u32 s7, s7, s3
	s_bcnt1_i32_b64 s3, s[8:9]
	s_lshl1_add_u32 s7, s7, s3
	s_cmp_lt_u32 s7, s11
	s_cselect_b32 s4, s4, s6
	s_lshr_b32 s5, s5, 1
	s_cmp_lg_u32 s5, 0x400000
	s_cbranch_scc1 .Ltk0_a28
	s_mov_b32 s10, s4
	s_add_u32 s6, s4, 0x800000
	s_cbranch_scc1 .Ltk0_f28
	s_mov_b32 s5, 0

.Ltk0_a24:
	s_or_b32 s6, s4, s5
	v_cmp_le_u32_e64 s[8:9], s6, v179
	v_cmp_le_u32_e64 s[12:13], s6, v187
	v_cmp_le_u32_e64 s[16:17], s6, v192
	v_cndmask_b32_e64 v8, 0, 1, s[8:9]
	v_cmp_le_u32_e64 s[8:9], s6, v196
	v_addc_co_u32_e64 v8, s[20:21], 0, v8, s[12:13]
	v_cmp_le_u32_e64 s[12:13], s6, v207
	v_addc_co_u32_e64 v8, s[20:21], 0, v8, s[16:17]
	v_cmp_le_u32_e64 s[16:17], s6, v211
	v_addc_co_u32_e64 v8, s[20:21], 0, v8, s[8:9]
	v_addc_co_u32_e64 v8, s[20:21], 0, v8, s[12:13]
	v_addc_co_u32_e64 v8, s[20:21], 0, v8, s[16:17]
	v_and_b32_e32 v9, 4, v8
	v_cmp_ne_u32_e64 s[16:17], 0, v9
	v_and_b32_e32 v9, 2, v8
	v_cmp_ne_u32_e64 s[12:13], 0, v9
	v_and_b32_e32 v9, 1, v8
	v_cmp_ne_u32_e64 s[8:9], 0, v9
	s_bcnt1_i32_b64 s7, s[16:17]
	s_bcnt1_i32_b64 s3, s[12:13]
	s_lshl1_add_u32 s7, s7, s3
	s_bcnt1_i32_b64 s3, s[8:9]
	s_lshl1_add_u32 s7, s7, s3
	s_cmp_lt_u32 s7, s11
	s_cselect_b32 s4, s4, s6
	s_lshr_b32 s5, s5, 1
	s_cmp_lg_u32 s5, 0x400000
	s_cbranch_scc1 .Ltk0_a24
	s_mov_b32 s10, s4
	s_add_u32 s6, s4, 0x800000
	s_cbranch_scc1 .Ltk0_f24
	s_mov_b32 s5, 0

.Ltk0_a20:
	s_or_b32 s6, s4, s5
	v_cmp_le_u32_e64 s[8:9], s6, v179
	v_cmp_le_u32_e64 s[12:13], s6, v187
	v_cmp_le_u32_e64 s[16:17], s6, v192
	v_cndmask_b32_e64 v8, 0, 1, s[8:9]
	v_cmp_le_u32_e64 s[8:9], s6, v196
	v_addc_co_u32_e64 v8, s[20:21], 0, v8, s[12:13]
	v_cmp_le_u32_e64 s[12:13], s6, v207
	v_addc_co_u32_e64 v8, s[20:21], 0, v8, s[16:17]
	v_addc_co_u32_e64 v8, s[20:21], 0, v8, s[8:9]
	v_addc_co_u32_e64 v8, s[20:21], 0, v8, s[12:13]
	v_and_b32_e32 v9, 4, v8
	v_cmp_ne_u32_e64 s[16:17], 0, v9
	v_and_b32_e32 v9, 2, v8
	v_cmp_ne_u32_e64 s[12:13], 0, v9
	v_and_b32_e32 v9, 1, v8
	v_cmp_ne_u32_e64 s[8:9], 0, v9
	s_bcnt1_i32_b64 s7, s[16:17]
	s_bcnt1_i32_b64 s3, s[12:13]
	s_lshl1_add_u32 s7, s7, s3
	s_bcnt1_i32_b64 s3, s[8:9]
	s_lshl1_add_u32 s7, s7, s3
	s_cmp_lt_u32 s7, s11
	s_cselect_b32 s4, s4, s6
	s_lshr_b32 s5, s5, 1
	s_cmp_lg_u32 s5, 0x400000
	s_cbranch_scc1 .Ltk0_a20
	s_mov_b32 s10, s4
	s_add_u32 s6, s4, 0x800000
	s_cbranch_scc1 .Ltk0_f20
	s_mov_b32 s5, 0

.Ltk1_a32:
	s_or_b32 s6, s4, s5
	v_cmp_le_u32_e64 s[8:9], s6, v142
	v_cmp_le_u32_e64 s[12:13], s6, v150
	v_cmp_le_u32_e64 s[16:17], s6, v155
	v_cndmask_b32_e64 v8, 0, 1, s[8:9]
	v_cmp_le_u32_e64 s[8:9], s6, v159
	v_addc_co_u32_e64 v8, s[20:21], 0, v8, s[12:13]
	v_cmp_le_u32_e64 s[12:13], s6, v171
	v_addc_co_u32_e64 v8, s[20:21], 0, v8, s[16:17]
	v_cmp_le_u32_e64 s[16:17], s6, v184
	v_addc_co_u32_e64 v8, s[20:21], 0, v8, s[8:9]
	v_cmp_le_u32_e64 s[8:9], s6, v199
	v_addc_co_u32_e64 v8, s[20:21], 0, v8, s[12:13]
	v_cmp_le_u32_e64 s[12:13], s6, v204
	v_addc_co_u32_e64 v8, s[20:21], 0, v8, s[16:17]
	v_addc_co_u32_e64 v8, s[20:21], 0, v8, s[8:9]
	v_addc_co_u32_e64 v8, s[20:21], 0, v8, s[12:13]
	v_and_b32_e32 v9, 8, v8
	v_cmp_ne_u32_e64 s[18:19], 0, v9
	v_and_b32_e32 v9, 4, v8
	v_cmp_ne_u32_e64 s[16:17], 0, v9
	v_and_b32_e32 v9, 2, v8
	v_cmp_ne_u32_e64 s[12:13], 0, v9
	v_and_b32_e32 v9, 1, v8
	v_cmp_ne_u32_e64 s[8:9], 0, v9
	s_bcnt1_i32_b64 s7, s[18:19]
	s_bcnt1_i32_b64 s3, s[16:17]
	s_lshl1_add_u32 s7, s7, s3
	s_bcnt1_i32_b64 s3, s[12:13]
	s_lshl1_add_u32 s7, s7, s3
	s_bcnt1_i32_b64 s3, s[8:9]
	s_lshl1_add_u32 s7, s7, s3
	s_cmp_lt_u32 s7, s11
	s_cselect_b32 s4, s4, s6
	s_lshr_b32 s5, s5, 1
	s_cmp_lg_u32 s5, 0x400000
	s_cbranch_scc1 .Ltk1_a32
	s_mov_b32 s10, s4
	s_add_u32 s6, s4, 0x800000
	s_cbranch_scc1 .Ltk1_f32
	s_mov_b32 s5, 0

.Ltk1_a28:
	s_or_b32 s6, s4, s5
	v_cmp_le_u32_e64 s[8:9], s6, v142
	v_cmp_le_u32_e64 s[12:13], s6, v150
	v_cmp_le_u32_e64 s[16:17], s6, v155
	v_cndmask_b32_e64 v8, 0, 1, s[8:9]
	v_cmp_le_u32_e64 s[8:9], s6, v159
	v_addc_co_u32_e64 v8, s[20:21], 0, v8, s[12:13]
	v_cmp_le_u32_e64 s[12:13], s6, v171
	v_addc_co_u32_e64 v8, s[20:21], 0, v8, s[16:17]
	v_cmp_le_u32_e64 s[16:17], s6, v184
	v_addc_co_u32_e64 v8, s[20:21], 0, v8, s[8:9]
	v_cmp_le_u32_e64 s[8:9], s6, v199
	v_addc_co_u32_e64 v8, s[20:21], 0, v8, s[12:13]
	v_addc_co_u32_e64 v8, s[20:21], 0, v8, s[16:17]
	v_addc_co_u32_e64 v8, s[20:21], 0, v8, s[8:9]
	v_and_b32_e32 v9, 4, v8
	v_cmp_ne_u32_e64 s[16:17], 0, v9
	v_and_b32_e32 v9, 2, v8
	v_cmp_ne_u32_e64 s[12:13], 0, v9
	v_and_b32_e32 v9, 1, v8
	v_cmp_ne_u32_e64 s[8:9], 0, v9
	s_bcnt1_i32_b64 s7, s[16:17]
	s_bcnt1_i32_b64 s3, s[12:13]
	s_lshl1_add_u32 s7, s7, s3
	s_bcnt1_i32_b64 s3, s[8:9]
	s_lshl1_add_u32 s7, s7, s3
	s_cmp_lt_u32 s7, s11
	s_cselect_b32 s4, s4, s6
	s_lshr_b32 s5, s5, 1
	s_cmp_lg_u32 s5, 0x400000
	s_cbranch_scc1 .Ltk1_a28
	s_mov_b32 s10, s4
	s_add_u32 s6, s4, 0x800000
	s_cbranch_scc1 .Ltk1_f28
	s_mov_b32 s5, 0

.Ltk1_a24:
	s_or_b32 s6, s4, s5
	v_cmp_le_u32_e64 s[8:9], s6, v142
	v_cmp_le_u32_e64 s[12:13], s6, v150
	v_cmp_le_u32_e64 s[16:17], s6, v155
	v_cndmask_b32_e64 v8, 0, 1, s[8:9]
	v_cmp_le_u32_e64 s[8:9], s6, v159
	v_addc_co_u32_e64 v8, s[20:21], 0, v8, s[12:13]
	v_cmp_le_u32_e64 s[12:13], s6, v171
	v_addc_co_u32_e64 v8, s[20:21], 0, v8, s[16:17]
	v_cmp_le_u32_e64 s[16:17], s6, v184
	v_addc_co_u32_e64 v8, s[20:21], 0, v8, s[8:9]
	v_addc_co_u32_e64 v8, s[20:21], 0, v8, s[12:13]
	v_addc_co_u32_e64 v8, s[20:21], 0, v8, s[16:17]
	v_and_b32_e32 v9, 4, v8
	v_cmp_ne_u32_e64 s[16:17], 0, v9
	v_and_b32_e32 v9, 2, v8
	v_cmp_ne_u32_e64 s[12:13], 0, v9
	v_and_b32_e32 v9, 1, v8
	v_cmp_ne_u32_e64 s[8:9], 0, v9
	s_bcnt1_i32_b64 s7, s[16:17]
	s_bcnt1_i32_b64 s3, s[12:13]
	s_lshl1_add_u32 s7, s7, s3
	s_bcnt1_i32_b64 s3, s[8:9]
	s_lshl1_add_u32 s7, s7, s3
	s_cmp_lt_u32 s7, s11
	s_cselect_b32 s4, s4, s6
	s_lshr_b32 s5, s5, 1
	s_cmp_lg_u32 s5, 0x400000
	s_cbranch_scc1 .Ltk1_a24
	s_mov_b32 s10, s4
	s_add_u32 s6, s4, 0x800000
	s_cbranch_scc1 .Ltk1_f24
	s_mov_b32 s5, 0

.Ltk1_a20:
	s_or_b32 s6, s4, s5
	v_cmp_le_u32_e64 s[8:9], s6, v142
	v_cmp_le_u32_e64 s[12:13], s6, v150
	v_cmp_le_u32_e64 s[16:17], s6, v155
	v_cndmask_b32_e64 v8, 0, 1, s[8:9]
	v_cmp_le_u32_e64 s[8:9], s6, v159
	v_addc_co_u32_e64 v8, s[20:21], 0, v8, s[12:13]
	v_cmp_le_u32_e64 s[12:13], s6, v171
	v_addc_co_u32_e64 v8, s[20:21], 0, v8, s[16:17]
	v_addc_co_u32_e64 v8, s[20:21], 0, v8, s[8:9]
	v_addc_co_u32_e64 v8, s[20:21], 0, v8, s[12:13]
	v_and_b32_e32 v9, 4, v8
	v_cmp_ne_u32_e64 s[16:17], 0, v9
	v_and_b32_e32 v9, 2, v8
	v_cmp_ne_u32_e64 s[12:13], 0, v9
	v_and_b32_e32 v9, 1, v8
	v_cmp_ne_u32_e64 s[8:9], 0, v9
	s_bcnt1_i32_b64 s7, s[16:17]
	s_bcnt1_i32_b64 s3, s[12:13]
	s_lshl1_add_u32 s7, s7, s3
	s_bcnt1_i32_b64 s3, s[8:9]
	s_lshl1_add_u32 s7, s7, s3
	s_cmp_lt_u32 s7, s11
	s_cselect_b32 s4, s4, s6
	s_lshr_b32 s5, s5, 1
	s_cmp_lg_u32 s5, 0x400000
	s_cbranch_scc1 .Ltk1_a20
	s_mov_b32 s10, s4
	s_add_u32 s6, s4, 0x800000
	s_cbranch_scc1 .Ltk1_f20
	s_mov_b32 s5, 0

.Ltk2_a32:
	s_or_b32 s6, s4, s5
	v_cmp_le_u32_e64 s[8:9], s6, v113
	v_cmp_le_u32_e64 s[12:13], s6, v121
	v_cmp_le_u32_e64 s[16:17], s6, v126
	v_cndmask_b32_e64 v8, 0, 1, s[8:9]
	v_cmp_le_u32_e64 s[8:9], s6, v130
	v_addc_co_u32_e64 v8, s[20:21], 0, v8, s[12:13]
	v_cmp_le_u32_e64 s[12:13], s6, v139
	v_addc_co_u32_e64 v8, s[20:21], 0, v8, s[16:17]
	v_cmp_le_u32_e64 s[16:17], s6, v147
	v_addc_co_u32_e64 v8, s[20:21], 0, v8, s[8:9]
	v_cmp_le_u32_e64 s[8:9], s6, v163
	v_addc_co_u32_e64 v8, s[20:21], 0, v8, s[12:13]
	v_cmp_le_u32_e64 s[12:13], s6, v168
	v_addc_co_u32_e64 v8, s[20:21], 0, v8, s[16:17]
	v_addc_co_u32_e64 v8, s[20:21], 0, v8, s[8:9]
	v_addc_co_u32_e64 v8, s[20:21], 0, v8, s[12:13]
	v_and_b32_e32 v9, 8, v8
	v_cmp_ne_u32_e64 s[18:19], 0, v9
	v_and_b32_e32 v9, 4, v8
	v_cmp_ne_u32_e64 s[16:17], 0, v9
	v_and_b32_e32 v9, 2, v8
	v_cmp_ne_u32_e64 s[12:13], 0, v9
	v_and_b32_e32 v9, 1, v8
	v_cmp_ne_u32_e64 s[8:9], 0, v9
	s_bcnt1_i32_b64 s7, s[18:19]
	s_bcnt1_i32_b64 s3, s[16:17]
	s_lshl1_add_u32 s7, s7, s3
	s_bcnt1_i32_b64 s3, s[12:13]
	s_lshl1_add_u32 s7, s7, s3
	s_bcnt1_i32_b64 s3, s[8:9]
	s_lshl1_add_u32 s7, s7, s3
	s_cmp_lt_u32 s7, s11
	s_cselect_b32 s4, s4, s6
	s_lshr_b32 s5, s5, 1
	s_cmp_lg_u32 s5, 0x400000
	s_cbranch_scc1 .Ltk2_a32
	s_mov_b32 s10, s4
	s_add_u32 s6, s4, 0x800000
	s_cbranch_scc1 .Ltk2_f32
	s_mov_b32 s5, 0

.Ltk2_a28:
	s_or_b32 s6, s4, s5
	v_cmp_le_u32_e64 s[8:9], s6, v113
	v_cmp_le_u32_e64 s[12:13], s6, v121
	v_cmp_le_u32_e64 s[16:17], s6, v126
	v_cndmask_b32_e64 v8, 0, 1, s[8:9]
	v_cmp_le_u32_e64 s[8:9], s6, v130
	v_addc_co_u32_e64 v8, s[20:21], 0, v8, s[12:13]
	v_cmp_le_u32_e64 s[12:13], s6, v139
	v_addc_co_u32_e64 v8, s[20:21], 0, v8, s[16:17]
	v_cmp_le_u32_e64 s[16:17], s6, v147
	v_addc_co_u32_e64 v8, s[20:21], 0, v8, s[8:9]
	v_cmp_le_u32_e64 s[8:9], s6, v163
	v_addc_co_u32_e64 v8, s[20:21], 0, v8, s[12:13]
	v_addc_co_u32_e64 v8, s[20:21], 0, v8, s[16:17]
	v_addc_co_u32_e64 v8, s[20:21], 0, v8, s[8:9]
	v_and_b32_e32 v9, 4, v8
	v_cmp_ne_u32_e64 s[16:17], 0, v9
	v_and_b32_e32 v9, 2, v8
	v_cmp_ne_u32_e64 s[12:13], 0, v9
	v_and_b32_e32 v9, 1, v8
	v_cmp_ne_u32_e64 s[8:9], 0, v9
	s_bcnt1_i32_b64 s7, s[16:17]
	s_bcnt1_i32_b64 s3, s[12:13]
	s_lshl1_add_u32 s7, s7, s3
	s_bcnt1_i32_b64 s3, s[8:9]
	s_lshl1_add_u32 s7, s7, s3
	s_cmp_lt_u32 s7, s11
	s_cselect_b32 s4, s4, s6
	s_lshr_b32 s5, s5, 1
	s_cmp_lg_u32 s5, 0x400000
	s_cbranch_scc1 .Ltk2_a28
	s_mov_b32 s10, s4
	s_add_u32 s6, s4, 0x800000
	s_cbranch_scc1 .Ltk2_f28
	s_mov_b32 s5, 0

.Ltk2_a24:
	s_or_b32 s6, s4, s5
	v_cmp_le_u32_e64 s[8:9], s6, v113
	v_cmp_le_u32_e64 s[12:13], s6, v121
	v_cmp_le_u32_e64 s[16:17], s6, v126
	v_cndmask_b32_e64 v8, 0, 1, s[8:9]
	v_cmp_le_u32_e64 s[8:9], s6, v130
	v_addc_co_u32_e64 v8, s[20:21], 0, v8, s[12:13]
	v_cmp_le_u32_e64 s[12:13], s6, v139
	v_addc_co_u32_e64 v8, s[20:21], 0, v8, s[16:17]
	v_cmp_le_u32_e64 s[16:17], s6, v147
	v_addc_co_u32_e64 v8, s[20:21], 0, v8, s[8:9]
	v_addc_co_u32_e64 v8, s[20:21], 0, v8, s[12:13]
	v_addc_co_u32_e64 v8, s[20:21], 0, v8, s[16:17]
	v_and_b32_e32 v9, 4, v8
	v_cmp_ne_u32_e64 s[16:17], 0, v9
	v_and_b32_e32 v9, 2, v8
	v_cmp_ne_u32_e64 s[12:13], 0, v9
	v_and_b32_e32 v9, 1, v8
	v_cmp_ne_u32_e64 s[8:9], 0, v9
	s_bcnt1_i32_b64 s7, s[16:17]
	s_bcnt1_i32_b64 s3, s[12:13]
	s_lshl1_add_u32 s7, s7, s3
	s_bcnt1_i32_b64 s3, s[8:9]
	s_lshl1_add_u32 s7, s7, s3
	s_cmp_lt_u32 s7, s11
	s_cselect_b32 s4, s4, s6
	s_lshr_b32 s5, s5, 1
	s_cmp_lg_u32 s5, 0x400000
	s_cbranch_scc1 .Ltk2_a24
	s_mov_b32 s10, s4
	s_add_u32 s6, s4, 0x800000
	s_cbranch_scc1 .Ltk2_f24
	s_mov_b32 s5, 0

.Ltk2_a20:
	s_or_b32 s6, s4, s5
	v_cmp_le_u32_e64 s[8:9], s6, v113
	v_cmp_le_u32_e64 s[12:13], s6, v121
	v_cmp_le_u32_e64 s[16:17], s6, v126
	v_cndmask_b32_e64 v8, 0, 1, s[8:9]
	v_cmp_le_u32_e64 s[8:9], s6, v130
	v_addc_co_u32_e64 v8, s[20:21], 0, v8, s[12:13]
	v_cmp_le_u32_e64 s[12:13], s6, v139
	v_addc_co_u32_e64 v8, s[20:21], 0, v8, s[16:17]
	v_addc_co_u32_e64 v8, s[20:21], 0, v8, s[8:9]
	v_addc_co_u32_e64 v8, s[20:21], 0, v8, s[12:13]
	v_and_b32_e32 v9, 4, v8
	v_cmp_ne_u32_e64 s[16:17], 0, v9
	v_and_b32_e32 v9, 2, v8
	v_cmp_ne_u32_e64 s[12:13], 0, v9
	v_and_b32_e32 v9, 1, v8
	v_cmp_ne_u32_e64 s[8:9], 0, v9
	s_bcnt1_i32_b64 s7, s[16:17]
	s_bcnt1_i32_b64 s3, s[12:13]
	s_lshl1_add_u32 s7, s7, s3
	s_bcnt1_i32_b64 s3, s[8:9]
	s_lshl1_add_u32 s7, s7, s3
	s_cmp_lt_u32 s7, s11
	s_cselect_b32 s4, s4, s6
	s_lshr_b32 s5, s5, 1
	s_cmp_lg_u32 s5, 0x400000
	s_cbranch_scc1 .Ltk2_a20
	s_mov_b32 s10, s4
	s_add_u32 s6, s4, 0x800000
	s_cbranch_scc1 .Ltk2_f20
	s_mov_b32 s5, 0

.Ltk3_a32:
	s_or_b32 s6, s4, s5
	v_cmp_le_u32_e64 s[8:9], s6, v94
	v_cmp_le_u32_e64 s[12:13], s6, v98
	v_cmp_le_u32_e64 s[16:17], s6, v102
	v_cndmask_b32_e64 v8, 0, 1, s[8:9]
	v_cmp_le_u32_e64 s[8:9], s6, v106
	v_addc_co_u32_e64 v8, s[20:21], 0, v8, s[12:13]
	v_cmp_le_u32_e64 s[12:13], s6, v110
	v_addc_co_u32_e64 v8, s[20:21], 0, v8, s[16:17]
	v_cmp_le_u32_e64 s[16:17], s6, v118
	v_addc_co_u32_e64 v8, s[20:21], 0, v8, s[8:9]
	v_cmp_le_u32_e64 s[8:9], s6, v90
	v_addc_co_u32_e64 v8, s[20:21], 0, v8, s[12:13]
	v_cmp_le_u32_e64 s[12:13], s6, v136
	v_addc_co_u32_e64 v8, s[20:21], 0, v8, s[16:17]
	v_addc_co_u32_e64 v8, s[20:21], 0, v8, s[8:9]
	v_addc_co_u32_e64 v8, s[20:21], 0, v8, s[12:13]
	v_and_b32_e32 v9, 8, v8
	v_cmp_ne_u32_e64 s[18:19], 0, v9
	v_and_b32_e32 v9, 4, v8
	v_cmp_ne_u32_e64 s[16:17], 0, v9
	v_and_b32_e32 v9, 2, v8
	v_cmp_ne_u32_e64 s[12:13], 0, v9
	v_and_b32_e32 v9, 1, v8
	v_cmp_ne_u32_e64 s[8:9], 0, v9
	s_bcnt1_i32_b64 s7, s[18:19]
	s_bcnt1_i32_b64 s3, s[16:17]
	s_lshl1_add_u32 s7, s7, s3
	s_bcnt1_i32_b64 s3, s[12:13]
	s_lshl1_add_u32 s7, s7, s3
	s_bcnt1_i32_b64 s3, s[8:9]
	s_lshl1_add_u32 s7, s7, s3
	s_cmp_lt_u32 s7, s11
	s_cselect_b32 s4, s4, s6
	s_lshr_b32 s5, s5, 1
	s_cmp_lg_u32 s5, 0x400000
	s_cbranch_scc1 .Ltk3_a32
	s_mov_b32 s10, s4
	s_add_u32 s6, s4, 0x800000
	s_cbranch_scc1 .Ltk3_f32
	s_mov_b32 s5, 0

.Ltk3_a28:
	s_or_b32 s6, s4, s5
	v_cmp_le_u32_e64 s[8:9], s6, v94
	v_cmp_le_u32_e64 s[12:13], s6, v98
	v_cmp_le_u32_e64 s[16:17], s6, v102
	v_cndmask_b32_e64 v8, 0, 1, s[8:9]
	v_cmp_le_u32_e64 s[8:9], s6, v106
	v_addc_co_u32_e64 v8, s[20:21], 0, v8, s[12:13]
	v_cmp_le_u32_e64 s[12:13], s6, v110
	v_addc_co_u32_e64 v8, s[20:21], 0, v8, s[16:17]
	v_cmp_le_u32_e64 s[16:17], s6, v118
	v_addc_co_u32_e64 v8, s[20:21], 0, v8, s[8:9]
	v_cmp_le_u32_e64 s[8:9], s6, v90
	v_addc_co_u32_e64 v8, s[20:21], 0, v8, s[12:13]
	v_addc_co_u32_e64 v8, s[20:21], 0, v8, s[16:17]
	v_addc_co_u32_e64 v8, s[20:21], 0, v8, s[8:9]
	v_and_b32_e32 v9, 4, v8
	v_cmp_ne_u32_e64 s[16:17], 0, v9
	v_and_b32_e32 v9, 2, v8
	v_cmp_ne_u32_e64 s[12:13], 0, v9
	v_and_b32_e32 v9, 1, v8
	v_cmp_ne_u32_e64 s[8:9], 0, v9
	s_bcnt1_i32_b64 s7, s[16:17]
	s_bcnt1_i32_b64 s3, s[12:13]
	s_lshl1_add_u32 s7, s7, s3
	s_bcnt1_i32_b64 s3, s[8:9]
	s_lshl1_add_u32 s7, s7, s3
	s_cmp_lt_u32 s7, s11
	s_cselect_b32 s4, s4, s6
	s_lshr_b32 s5, s5, 1
	s_cmp_lg_u32 s5, 0x400000
	s_cbranch_scc1 .Ltk3_a28
	s_mov_b32 s10, s4
	s_add_u32 s6, s4, 0x800000
	s_cbranch_scc1 .Ltk3_f28
	s_mov_b32 s5, 0

.Ltk3_a24:
	s_or_b32 s6, s4, s5
	v_cmp_le_u32_e64 s[8:9], s6, v94
	v_cmp_le_u32_e64 s[12:13], s6, v98
	v_cmp_le_u32_e64 s[16:17], s6, v102
	v_cndmask_b32_e64 v8, 0, 1, s[8:9]
	v_cmp_le_u32_e64 s[8:9], s6, v106
	v_addc_co_u32_e64 v8, s[20:21], 0, v8, s[12:13]
	v_cmp_le_u32_e64 s[12:13], s6, v110
	v_addc_co_u32_e64 v8, s[20:21], 0, v8, s[16:17]
	v_cmp_le_u32_e64 s[16:17], s6, v118
	v_addc_co_u32_e64 v8, s[20:21], 0, v8, s[8:9]
	v_addc_co_u32_e64 v8, s[20:21], 0, v8, s[12:13]
	v_addc_co_u32_e64 v8, s[20:21], 0, v8, s[16:17]
	v_and_b32_e32 v9, 4, v8
	v_cmp_ne_u32_e64 s[16:17], 0, v9
	v_and_b32_e32 v9, 2, v8
	v_cmp_ne_u32_e64 s[12:13], 0, v9
	v_and_b32_e32 v9, 1, v8
	v_cmp_ne_u32_e64 s[8:9], 0, v9
	s_bcnt1_i32_b64 s7, s[16:17]
	s_bcnt1_i32_b64 s3, s[12:13]
	s_lshl1_add_u32 s7, s7, s3
	s_bcnt1_i32_b64 s3, s[8:9]
	s_lshl1_add_u32 s7, s7, s3
	s_cmp_lt_u32 s7, s11
	s_cselect_b32 s4, s4, s6
	s_lshr_b32 s5, s5, 1
	s_cmp_lg_u32 s5, 0x400000
	s_cbranch_scc1 .Ltk3_a24
	s_mov_b32 s10, s4
	s_add_u32 s6, s4, 0x800000
	s_cbranch_scc1 .Ltk3_f24
	s_mov_b32 s5, 0

.Ltk3_a20:
	s_or_b32 s6, s4, s5
	v_cmp_le_u32_e64 s[8:9], s6, v94
	v_cmp_le_u32_e64 s[12:13], s6, v98
	v_cmp_le_u32_e64 s[16:17], s6, v102
	v_cndmask_b32_e64 v8, 0, 1, s[8:9]
	v_cmp_le_u32_e64 s[8:9], s6, v106
	v_addc_co_u32_e64 v8, s[20:21], 0, v8, s[12:13]
	v_cmp_le_u32_e64 s[12:13], s6, v110
	v_addc_co_u32_e64 v8, s[20:21], 0, v8, s[16:17]
	v_addc_co_u32_e64 v8, s[20:21], 0, v8, s[8:9]
	v_addc_co_u32_e64 v8, s[20:21], 0, v8, s[12:13]
	v_and_b32_e32 v9, 4, v8
	v_cmp_ne_u32_e64 s[16:17], 0, v9
	v_and_b32_e32 v9, 2, v8
	v_cmp_ne_u32_e64 s[12:13], 0, v9
	v_and_b32_e32 v9, 1, v8
	v_cmp_ne_u32_e64 s[8:9], 0, v9
	s_bcnt1_i32_b64 s7, s[16:17]
	s_bcnt1_i32_b64 s3, s[12:13]
	s_lshl1_add_u32 s7, s7, s3
	s_bcnt1_i32_b64 s3, s[8:9]
	s_lshl1_add_u32 s7, s7, s3
	s_cmp_lt_u32 s7, s11
	s_cselect_b32 s4, s4, s6
	s_lshr_b32 s5, s5, 1
	s_cmp_lg_u32 s5, 0x400000
	s_cbranch_scc1 .Ltk3_a20
	s_mov_b32 s10, s4
	s_add_u32 s6, s4, 0x800000
	s_cbranch_scc1 .Ltk3_f20
	s_mov_b32 s5, 0
